# g16: g13 + P1 GEMM: per-segment setprio flips removed, trailing wave half at static priority 1
# baseline (speedup 1.0000x reference)
.LBB0_76:
	s_cmp_lt_i32 s60, 2
	s_cselect_b64 s[4:5], -1, 0
	s_and_b64 s[0:1], s[4:5], s[0:1]
	s_andn2_b64 vcc, exec, s[0:1]
	s_cbranch_vccnz .LBB0_98
	s_add_u32 s6, s96, 0x34000000
	s_addc_u32 s7, s97, 0
	v_readlane_b32 s8, v254, 0
	v_readfirstlane_b32 s5, v0
	v_lshrrev_b32_e32 v151, 2, v0
	v_lshrrev_b32_e32 v1, 3, v0
	s_cmpk_gt_i32 s8, 0xaff
	v_and_b32_e32 v150, 15, v0
	v_readlane_b32 s9, v254, 1
	s_cbranch_scc1 .LBB0_93
	s_cmp_lt_u32 s82, 4
	s_cbranch_scc1 .Lp1_noprio
	s_setprio 1
.Lp1_noprio:
	v_lshrrev_b32_e32 v2, 5, v0
	v_lshlrev_b32_e32 v4, 1, v151
	v_and_b32_e32 v2, 4, v2
	v_bfe_u32 v3, v0, 2, 2
	v_and_b32_e32 v4, 24, v4
	v_or3_b32 v2, v2, v3, v4
	v_lshlrev_b32_e32 v3, 4, v0
	v_or_b32_e32 v10, 0x2000, v3
	s_add_u32 s34, s96, 0x200000
	v_lshrrev_b32_e32 v4, 7, v10
	s_movk_i32 s4, 0x60
	v_readlane_b32 s8, v254, 0
	s_addc_u32 s35, s97, 0
	v_and_or_b32 v5, v4, s4, v2
	v_bfe_u32 v13, v0, 2, 4
	s_movk_i32 s4, 0x70
	s_ashr_i32 s37, s8, 31
	v_and_or_b32 v4, v4, s4, v13
	s_lshr_b32 s4, s37, 29
	s_add_i32 s4, s8, s4
	s_lshr_b32 s12, s5, 6
	s_mov_b32 s2, s8
	s_ashr_i32 s8, s4, 3
	s_and_b32 s4, s4, -8
	s_lshr_b32 s16, s5, 8
	s_lshl_b32 s36, s12, 10
	s_sub_i32 s4, s2, s4
	v_readlane_b32 s9, v254, 1
	s_cmp_lt_i32 s4, 0
	s_movk_i32 s38, 0x161
	s_cselect_b32 s9, s38, 0x160
	s_mul_i32 s4, s4, s9
	s_add_i32 s4, s4, s8
	s_mul_hi_i32 s8, s4, 0x2e8ba2e9
	s_lshr_b32 s9, s8, 31
	s_ashr_i32 s8, s8, 5
	s_add_i32 s8, s8, s9
	s_lshl_b32 s9, s8, 2
	s_mulk_i32 s8, 0xb0
	s_sub_i32 s8, s4, s8
	s_sext_i32_i16 s4, s8
	s_bfe_u32 s4, s4, 0x2001d
	s_add_i32 s10, s8, s4
	s_sext_i32_i16 s4, s10
	s_and_b32 s10, s10, 0xfffc
	s_sub_i32 s8, s8, s10
	s_sext_i32_i16 s8, s8
	s_lshr_b32 s4, s4, 2
	s_add_i32 s24, s9, s8
	s_ashr_i32 s25, s24, 31
	s_bfe_i64 s[10:11], s[4:5], 0x100000
	v_and_b32_e32 v6, 32, v0
	s_lshl_b64 s[8:9], s[24:25], 20
	s_lshl_b64 s[10:11], s[10:11], 20
	v_bitop3_b32 v11, v3, v6, 48 bitop3:0x6c
	v_and_b32_e32 v12, 64, v0
	s_add_u32 s28, s34, s10
	v_or_b32_e32 v3, v11, v12
	v_and_or_b32 v2, v1, 32, v2
	s_addc_u32 s29, s35, s11
	s_add_i32 s25, s36, 0
	v_lshl_or_b32 v134, v2, 12, v3
	s_add_i32 m0, s25, 0x10000
	v_lshl_or_b32 v130, v5, 12, v3
	global_load_lds_dwordx4 v134, s[28:29]
	s_add_i32 m0, s25, 0x12000
	s_add_u32 s10, s28, 0x80000
	global_load_lds_dwordx4 v130, s[28:29]
	s_addc_u32 s11, s29, 0
	s_add_i32 m0, s25, 0x14000
	v_and_or_b32 v2, v1, 48, v13
	global_load_lds_dwordx4 v134, s[10:11]
	s_add_i32 m0, s25, 0x16000
	s_add_u32 s26, s6, s8
	s_addc_u32 s27, s7, s9
	s_add_i32 s39, s25, 0x2000
	v_lshl_or_b32 v136, v2, 12, v3
	global_load_lds_dwordx4 v130, s[10:11]
	s_mov_b32 m0, s25
	s_add_u32 s8, s26, 0x80000
	v_lshl_or_b32 v132, v4, 12, v3
	global_load_lds_dwordx4 v136, s[26:27]
	s_mov_b32 m0, s39
	s_addc_u32 s9, s27, 0
	s_add_i32 s40, s25, 0x4000
	global_load_lds_dwordx4 v132, s[26:27]
	s_mov_b32 m0, s40
	s_add_i32 s41, s25, 0x6000
	global_load_lds_dwordx4 v136, s[8:9]
	s_mov_b32 m0, s41
	v_mov_b32_e32 v135, 0
	global_load_lds_dwordx4 v132, s[8:9]
	v_mov_b32_e32 v131, v135
	v_mov_b32_e32 v137, v135
	v_mov_b32_e32 v133, v135
	s_cmp_eq_u32 s16, 1
	s_mov_b32 s42, 0
	v_lshl_add_u64 v[8:9], s[28:29], 0, v[134:135]
	v_lshl_add_u64 v[6:7], s[28:29], 0, v[130:131]
	v_lshl_add_u64 v[2:3], s[26:27], 0, v[136:137]
	s_cselect_b64 s[8:9], -1, 0
	s_cmp_lg_u32 s16, 1
	v_lshl_add_u64 v[4:5], s[26:27], 0, v[132:133]
	s_cbranch_scc1 .LBB0_80
	s_barrier

.LBB0_85:
	s_ashr_i32 s19, s18, 31
	s_lshl_b64 s[20:21], s[18:19], 20
	s_add_u32 s20, s6, s20
	s_addc_u32 s21, s7, s21
	s_and_b64 s[22:23], s[4:5], exec
	s_cselect_b32 s19, s21, s27
	s_cselect_b32 s49, s20, s26
	s_ashr_i32 s17, s16, 31
	s_lshl_b64 s[22:23], s[16:17], 20
	s_add_u32 s22, s34, s22
	s_addc_u32 s23, s35, s23
	s_and_b64 s[30:31], s[4:5], exec
	s_cselect_b32 s17, s23, s29
	s_cselect_b32 s50, s22, s28
	s_add_u32 s26, s26, 0x80080
	s_addc_u32 s27, s27, 0
	s_add_u32 s51, s28, 0x100
	s_addc_u32 s52, s29, 0
	s_mov_b32 s53, -2
	ds_read_b128 v[146:149], v156
	ds_read_b128 v[170:173], v157
	ds_read_b128 v[174:177], v158
	ds_read_b128 v[178:181], v159
	ds_read_b128 v[182:185], v160
	ds_read_b128 v[188:191], v161
	ds_read_b128 v[192:195], v162
	ds_read_b128 v[196:199], v163
	s_add_u32 s28, s26, 0xfff80080
	s_addc_u32 s29, s27, -1
	s_cmp_eq_u32 s53, 28
	s_cselect_b32 s31, s19, s29
	s_cselect_b32 s30, s49, s28
	s_cselect_b32 s29, s17, s52
	s_cselect_b32 s28, s50, s51
	v_lshl_add_u64 v[232:233], s[26:27], 0, v[138:139]
	s_add_i32 m0, s25, 0xc000
	ds_read_b128 v[200:203], v164
	ds_read_b128 v[204:207], v164 offset:1024
	ds_read_b128 v[208:211], v164 offset:2048
	ds_read_b128 v[212:215], v164 offset:3072
	ds_read_b128 v[216:219], v164 offset:4096
	ds_read_b128 v[220:223], v164 offset:5120
	ds_read_b128 v[224:227], v164 offset:6144
	ds_read_b128 v[228:231], v164 offset:7168
	global_load_lds_dwordx4 v[232:233], off
	v_lshl_add_u64 v[232:233], s[26:27], 0, v[140:141]
	s_add_i32 m0, s25, 0xe000
	s_nop 0
	global_load_lds_dwordx4 v[232:233], off
	s_waitcnt vmcnt(8)
	s_waitcnt lgkmcnt(0)
	s_barrier
	s_waitcnt lgkmcnt(0)
	v_mfma_f32_16x16x32_bf16 v[126:129], v[146:149], v[200:203], 0
	v_mfma_f32_16x16x32_bf16 v[122:125], v[174:177], v[200:203], 0
	v_mfma_f32_16x16x32_bf16 v[118:121], v[146:149], v[208:211], 0
	v_mfma_f32_16x16x32_bf16 v[110:113], v[174:177], v[208:211], 0
	v_mfma_f32_16x16x32_bf16 v[102:105], v[146:149], v[216:219], 0
	v_mfma_f32_16x16x32_bf16 v[94:97], v[174:177], v[216:219], 0
	v_mfma_f32_16x16x32_bf16 v[86:89], v[146:149], v[224:227], 0
	v_mfma_f32_16x16x32_bf16 v[78:81], v[174:177], v[224:227], 0
	v_mfma_f32_16x16x32_bf16 v[126:129], v[170:173], v[204:207], v[126:129]
	v_mfma_f32_16x16x32_bf16 v[122:125], v[178:181], v[204:207], v[122:125]
	v_mfma_f32_16x16x32_bf16 v[118:121], v[170:173], v[212:215], v[118:121]
	v_mfma_f32_16x16x32_bf16 v[110:113], v[178:181], v[212:215], v[110:113]
	v_mfma_f32_16x16x32_bf16 v[102:105], v[170:173], v[220:223], v[102:105]
	v_mfma_f32_16x16x32_bf16 v[94:97], v[178:181], v[220:223], v[94:97]
	v_mfma_f32_16x16x32_bf16 v[86:89], v[170:173], v[228:231], v[86:89]
	v_mfma_f32_16x16x32_bf16 v[78:81], v[178:181], v[228:231], v[78:81]
	v_mfma_f32_16x16x32_bf16 v[114:117], v[182:185], v[200:203], 0
	v_mfma_f32_16x16x32_bf16 v[106:109], v[192:195], v[200:203], 0
	v_mfma_f32_16x16x32_bf16 v[98:101], v[182:185], v[208:211], 0
	v_mfma_f32_16x16x32_bf16 v[90:93], v[192:195], v[208:211], 0
	v_mfma_f32_16x16x32_bf16 v[82:85], v[182:185], v[216:219], 0
	v_mfma_f32_16x16x32_bf16 v[74:77], v[192:195], v[216:219], 0
	v_mfma_f32_16x16x32_bf16 v[70:73], v[182:185], v[224:227], 0
	v_mfma_f32_16x16x32_bf16 v[66:69], v[192:195], v[224:227], 0
	v_mfma_f32_16x16x32_bf16 v[114:117], v[188:191], v[204:207], v[114:117]
	v_mfma_f32_16x16x32_bf16 v[106:109], v[196:199], v[204:207], v[106:109]
	v_mfma_f32_16x16x32_bf16 v[98:101], v[188:191], v[212:215], v[98:101]
	v_mfma_f32_16x16x32_bf16 v[90:93], v[196:199], v[212:215], v[90:93]
	v_mfma_f32_16x16x32_bf16 v[82:85], v[188:191], v[220:223], v[82:85]
	v_mfma_f32_16x16x32_bf16 v[74:77], v[196:199], v[220:223], v[74:77]
	v_mfma_f32_16x16x32_bf16 v[70:73], v[188:191], v[228:231], v[70:73]
	v_mfma_f32_16x16x32_bf16 v[66:69], v[196:199], v[228:231], v[66:69]
	s_barrier
	s_add_i32 s54, s46, s36
	v_lshl_add_u64 v[232:233], s[28:29], 0, v[134:135]
	s_mov_b32 m0, s54
	ds_read_b128 v[200:203], v164 offset:16384
	ds_read_b128 v[204:207], v164 offset:17408
	ds_read_b128 v[208:211], v164 offset:18432
	ds_read_b128 v[212:215], v164 offset:19456
	ds_read_b128 v[216:219], v164 offset:20480
	ds_read_b128 v[220:223], v164 offset:21504
	ds_read_b128 v[224:227], v164 offset:22528
	ds_read_b128 v[228:231], v164 offset:23552
	global_load_lds_dwordx4 v[232:233], off
	s_add_i32 m0, s54, 0x2000
	s_add_u32 s54, s28, 0x80000
	v_lshl_add_u64 v[234:235], s[28:29], 0, v[130:131]
	s_addc_u32 s55, s29, 0
	s_add_i32 s57, s47, s36
	global_load_lds_dwordx4 v[234:235], off
	v_lshl_add_u64 v[236:237], s[54:55], 0, v[134:135]
	s_mov_b32 m0, s57
	v_lshl_add_u64 v[238:239], s[30:31], 0, v[132:133]
	global_load_lds_dwordx4 v[236:237], off
	v_lshl_add_u64 v[236:237], s[54:55], 0, v[130:131]
	s_add_i32 m0, s57, 0x2000
	s_nop 0
	global_load_lds_dwordx4 v[236:237], off
	v_lshl_add_u64 v[236:237], s[30:31], 0, v[136:137]
	s_mov_b32 m0, s25
	s_nop 0
	global_load_lds_dwordx4 v[236:237], off
	s_mov_b32 m0, s39
	s_nop 0
	global_load_lds_dwordx4 v[238:239], off
	s_waitcnt vmcnt(8)
	s_waitcnt lgkmcnt(0)
	s_barrier
	s_waitcnt lgkmcnt(0)
	v_mfma_f32_16x16x32_bf16 v[62:65], v[146:149], v[200:203], 0
	v_mfma_f32_16x16x32_bf16 v[58:61], v[174:177], v[200:203], 0
	v_mfma_f32_16x16x32_bf16 v[54:57], v[146:149], v[208:211], 0
	v_mfma_f32_16x16x32_bf16 v[46:49], v[174:177], v[208:211], 0
	v_mfma_f32_16x16x32_bf16 v[38:41], v[146:149], v[216:219], 0
	v_mfma_f32_16x16x32_bf16 v[30:33], v[174:177], v[216:219], 0
	v_mfma_f32_16x16x32_bf16 v[22:25], v[146:149], v[224:227], 0
	v_mfma_f32_16x16x32_bf16 v[14:17], v[174:177], v[224:227], 0
	v_mfma_f32_16x16x32_bf16 v[62:65], v[170:173], v[204:207], v[62:65]
	v_mfma_f32_16x16x32_bf16 v[58:61], v[178:181], v[204:207], v[58:61]
	v_mfma_f32_16x16x32_bf16 v[54:57], v[170:173], v[212:215], v[54:57]
	v_mfma_f32_16x16x32_bf16 v[46:49], v[178:181], v[212:215], v[46:49]
	v_mfma_f32_16x16x32_bf16 v[38:41], v[170:173], v[220:223], v[38:41]
	v_mfma_f32_16x16x32_bf16 v[30:33], v[178:181], v[220:223], v[30:33]
	v_mfma_f32_16x16x32_bf16 v[22:25], v[170:173], v[228:231], v[22:25]
	v_mfma_f32_16x16x32_bf16 v[14:17], v[178:181], v[228:231], v[14:17]
	v_mfma_f32_16x16x32_bf16 v[50:53], v[182:185], v[200:203], 0
	v_mfma_f32_16x16x32_bf16 v[42:45], v[192:195], v[200:203], 0
	v_mfma_f32_16x16x32_bf16 v[34:37], v[182:185], v[208:211], 0
	v_mfma_f32_16x16x32_bf16 v[26:29], v[192:195], v[208:211], 0
	v_mfma_f32_16x16x32_bf16 v[18:21], v[182:185], v[216:219], 0
	v_mfma_f32_16x16x32_bf16 v[10:13], v[192:195], v[216:219], 0
	v_mfma_f32_16x16x32_bf16 v[6:9], v[182:185], v[224:227], 0
	v_mfma_f32_16x16x32_bf16 v[2:5], v[192:195], v[224:227], 0
	v_mfma_f32_16x16x32_bf16 v[50:53], v[188:191], v[204:207], v[50:53]
	v_mfma_f32_16x16x32_bf16 v[42:45], v[196:199], v[204:207], v[42:45]
	v_mfma_f32_16x16x32_bf16 v[34:37], v[188:191], v[212:215], v[34:37]
	v_mfma_f32_16x16x32_bf16 v[26:29], v[196:199], v[212:215], v[26:29]
	v_mfma_f32_16x16x32_bf16 v[18:21], v[188:191], v[220:223], v[18:21]
	v_mfma_f32_16x16x32_bf16 v[10:13], v[196:199], v[220:223], v[10:13]
	v_mfma_f32_16x16x32_bf16 v[6:9], v[188:191], v[228:231], v[6:9]
	v_mfma_f32_16x16x32_bf16 v[2:5], v[196:199], v[228:231], v[2:5]
	s_barrier
	s_add_i32 s54, 0, 0x18000
	v_add_u32_e32 v146, s54, v152
	v_add_u32_e32 v169, s54, v153
	s_add_i32 s55, 0, 0x1c000
	ds_read_b128 v[146:149], v146
	ds_read_b128 v[170:173], v169
	ds_read_b128 v[174:177], v165
	ds_read_b128 v[178:181], v166
	v_add_u32_e32 v169, s55, v152
	v_add_u32_e32 v187, s55, v153
	ds_read_b128 v[182:185], v169
	ds_read_b128 v[188:191], v187
	ds_read_b128 v[192:195], v167
	ds_read_b128 v[196:199], v168
	s_add_u32 s30, s30, 0x80000
	s_addc_u32 s31, s31, 0
	s_mov_b32 m0, s40
	v_lshl_add_u64 v[240:241], s[30:31], 0, v[136:137]
	ds_read_b128 v[200:203], v164 offset:32768
	ds_read_b128 v[204:207], v164 offset:33792
	ds_read_b128 v[208:211], v164 offset:34816
	ds_read_b128 v[212:215], v164 offset:35840
	ds_read_b128 v[216:219], v164 offset:36864
	ds_read_b128 v[220:223], v164 offset:37888
	ds_read_b128 v[224:227], v164 offset:38912
	ds_read_b128 v[228:231], v164 offset:39936
	global_load_lds_dwordx4 v[240:241], off
	v_lshl_add_u64 v[240:241], s[30:31], 0, v[132:133]
	s_mov_b32 m0, s41
	s_nop 0
	global_load_lds_dwordx4 v[240:241], off
	s_waitcnt vmcnt(8)
	s_waitcnt lgkmcnt(0)
	s_barrier
	s_waitcnt lgkmcnt(0)
	v_mfma_f32_16x16x32_bf16 v[126:129], v[146:149], v[200:203], v[126:129]
	v_mfma_f32_16x16x32_bf16 v[122:125], v[174:177], v[200:203], v[122:125]
	v_mfma_f32_16x16x32_bf16 v[118:121], v[146:149], v[208:211], v[118:121]
	v_mfma_f32_16x16x32_bf16 v[110:113], v[174:177], v[208:211], v[110:113]
	v_mfma_f32_16x16x32_bf16 v[102:105], v[146:149], v[216:219], v[102:105]
	v_mfma_f32_16x16x32_bf16 v[94:97], v[174:177], v[216:219], v[94:97]
	v_mfma_f32_16x16x32_bf16 v[86:89], v[146:149], v[224:227], v[86:89]
	v_mfma_f32_16x16x32_bf16 v[78:81], v[174:177], v[224:227], v[78:81]
	v_mfma_f32_16x16x32_bf16 v[126:129], v[170:173], v[204:207], v[126:129]
	v_mfma_f32_16x16x32_bf16 v[122:125], v[178:181], v[204:207], v[122:125]
	v_mfma_f32_16x16x32_bf16 v[118:121], v[170:173], v[212:215], v[118:121]
	v_mfma_f32_16x16x32_bf16 v[110:113], v[178:181], v[212:215], v[110:113]
	v_mfma_f32_16x16x32_bf16 v[102:105], v[170:173], v[220:223], v[102:105]
	v_mfma_f32_16x16x32_bf16 v[94:97], v[178:181], v[220:223], v[94:97]
	v_mfma_f32_16x16x32_bf16 v[86:89], v[170:173], v[228:231], v[86:89]
	v_mfma_f32_16x16x32_bf16 v[78:81], v[178:181], v[228:231], v[78:81]
	v_mfma_f32_16x16x32_bf16 v[114:117], v[182:185], v[200:203], v[114:117]
	v_mfma_f32_16x16x32_bf16 v[106:109], v[192:195], v[200:203], v[106:109]
	v_mfma_f32_16x16x32_bf16 v[98:101], v[182:185], v[208:211], v[98:101]
	v_mfma_f32_16x16x32_bf16 v[90:93], v[192:195], v[208:211], v[90:93]
	v_mfma_f32_16x16x32_bf16 v[82:85], v[182:185], v[216:219], v[82:85]
	v_mfma_f32_16x16x32_bf16 v[74:77], v[192:195], v[216:219], v[74:77]
	v_mfma_f32_16x16x32_bf16 v[70:73], v[182:185], v[224:227], v[70:73]
	v_mfma_f32_16x16x32_bf16 v[66:69], v[192:195], v[224:227], v[66:69]
	v_mfma_f32_16x16x32_bf16 v[114:117], v[188:191], v[204:207], v[114:117]
	v_mfma_f32_16x16x32_bf16 v[106:109], v[196:199], v[204:207], v[106:109]
	v_mfma_f32_16x16x32_bf16 v[98:101], v[188:191], v[212:215], v[98:101]
	v_mfma_f32_16x16x32_bf16 v[90:93], v[196:199], v[212:215], v[90:93]
	v_mfma_f32_16x16x32_bf16 v[82:85], v[188:191], v[220:223], v[82:85]
	v_mfma_f32_16x16x32_bf16 v[74:77], v[196:199], v[220:223], v[74:77]
	v_mfma_f32_16x16x32_bf16 v[70:73], v[188:191], v[228:231], v[70:73]
	v_mfma_f32_16x16x32_bf16 v[66:69], v[196:199], v[228:231], v[66:69]
	s_barrier
	s_add_i32 s30, s54, s36
	v_lshl_add_u64 v[232:233], v[232:233], 0, s[12:13]
	s_mov_b32 m0, s30
	ds_read_b128 v[200:203], v164 offset:49152
	ds_read_b128 v[204:207], v164 offset:50176
	ds_read_b128 v[208:211], v164 offset:51200
	ds_read_b128 v[212:215], v164 offset:52224
	ds_read_b128 v[216:219], v164 offset:53248
	ds_read_b128 v[220:223], v164 offset:54272
	ds_read_b128 v[224:227], v164 offset:55296
	ds_read_b128 v[228:231], v164 offset:56320
	global_load_lds_dwordx4 v[232:233], off
	s_add_i32 m0, s30, 0x2000
	s_add_u32 s28, s28, 0x80080
	v_lshl_add_u64 v[232:233], v[234:235], 0, s[12:13]
	s_addc_u32 s29, s29, 0
	s_add_i32 s30, s55, s36
	global_load_lds_dwordx4 v[232:233], off
	v_lshl_add_u64 v[232:233], s[28:29], 0, v[134:135]
	s_mov_b32 m0, s30
	s_nop 0
	global_load_lds_dwordx4 v[232:233], off
	v_lshl_add_u64 v[232:233], s[28:29], 0, v[130:131]
	s_add_i32 m0, s30, 0x2000
	s_nop 0
	global_load_lds_dwordx4 v[232:233], off
	v_lshl_add_u64 v[232:233], v[236:237], 0, s[12:13]
	s_mov_b32 m0, s43
	s_nop 0
	global_load_lds_dwordx4 v[232:233], off
	v_lshl_add_u64 v[232:233], v[238:239], 0, s[12:13]
	s_mov_b32 m0, s44
	s_nop 0
	global_load_lds_dwordx4 v[232:233], off
	s_waitcnt vmcnt(8)
	s_waitcnt lgkmcnt(0)
	s_barrier
	s_waitcnt lgkmcnt(0)
	v_mfma_f32_16x16x32_bf16 v[62:65], v[146:149], v[200:203], v[62:65]
	v_mfma_f32_16x16x32_bf16 v[58:61], v[174:177], v[200:203], v[58:61]
	v_mfma_f32_16x16x32_bf16 v[54:57], v[146:149], v[208:211], v[54:57]
	v_mfma_f32_16x16x32_bf16 v[46:49], v[174:177], v[208:211], v[46:49]
	v_mfma_f32_16x16x32_bf16 v[38:41], v[146:149], v[216:219], v[38:41]
	v_mfma_f32_16x16x32_bf16 v[30:33], v[174:177], v[216:219], v[30:33]
	v_mfma_f32_16x16x32_bf16 v[22:25], v[146:149], v[224:227], v[22:25]
	v_mfma_f32_16x16x32_bf16 v[14:17], v[174:177], v[224:227], v[14:17]
	v_mfma_f32_16x16x32_bf16 v[62:65], v[170:173], v[204:207], v[62:65]
	v_mfma_f32_16x16x32_bf16 v[58:61], v[178:181], v[204:207], v[58:61]
	v_mfma_f32_16x16x32_bf16 v[54:57], v[170:173], v[212:215], v[54:57]
	v_mfma_f32_16x16x32_bf16 v[46:49], v[178:181], v[212:215], v[46:49]
	v_mfma_f32_16x16x32_bf16 v[38:41], v[170:173], v[220:223], v[38:41]
	v_mfma_f32_16x16x32_bf16 v[30:33], v[178:181], v[220:223], v[30:33]
	v_mfma_f32_16x16x32_bf16 v[22:25], v[170:173], v[228:231], v[22:25]
	v_mfma_f32_16x16x32_bf16 v[14:17], v[178:181], v[228:231], v[14:17]
	v_mfma_f32_16x16x32_bf16 v[50:53], v[182:185], v[200:203], v[50:53]
	v_mfma_f32_16x16x32_bf16 v[42:45], v[192:195], v[200:203], v[42:45]
	v_mfma_f32_16x16x32_bf16 v[34:37], v[182:185], v[208:211], v[34:37]
	v_mfma_f32_16x16x32_bf16 v[26:29], v[192:195], v[208:211], v[26:29]
	v_mfma_f32_16x16x32_bf16 v[18:21], v[182:185], v[216:219], v[18:21]
	v_mfma_f32_16x16x32_bf16 v[10:13], v[192:195], v[216:219], v[10:13]
	v_mfma_f32_16x16x32_bf16 v[6:9], v[182:185], v[224:227], v[6:9]
	v_mfma_f32_16x16x32_bf16 v[2:5], v[192:195], v[224:227], v[2:5]
	v_mfma_f32_16x16x32_bf16 v[50:53], v[188:191], v[204:207], v[50:53]
	v_mfma_f32_16x16x32_bf16 v[42:45], v[196:199], v[204:207], v[42:45]
	v_mfma_f32_16x16x32_bf16 v[34:37], v[188:191], v[212:215], v[34:37]
	v_mfma_f32_16x16x32_bf16 v[26:29], v[196:199], v[212:215], v[26:29]
	v_mfma_f32_16x16x32_bf16 v[18:21], v[188:191], v[220:223], v[18:21]
	v_mfma_f32_16x16x32_bf16 v[10:13], v[196:199], v[220:223], v[10:13]
	v_mfma_f32_16x16x32_bf16 v[6:9], v[188:191], v[228:231], v[6:9]
	v_mfma_f32_16x16x32_bf16 v[2:5], v[196:199], v[228:231], v[2:5]
	s_barrier
	s_add_i32 s53, s53, 2
	s_add_u32 s26, s26, 0x100
	s_addc_u32 s27, s27, 0
	s_add_u32 s51, s51, 0x100
	s_addc_u32 s52, s52, 0
.LBB0_86:
	ds_read_b128 v[146:149], v156
	ds_read_b128 v[170:173], v157
	ds_read_b128 v[174:177], v158
	ds_read_b128 v[178:181], v159
	ds_read_b128 v[182:185], v160
	ds_read_b128 v[188:191], v161
	ds_read_b128 v[192:195], v162
	ds_read_b128 v[196:199], v163
	s_add_u32 s28, s26, 0xfff80080
	s_addc_u32 s29, s27, -1
	s_cmp_eq_u32 s53, 28
	s_cselect_b32 s31, s19, s29
	s_cselect_b32 s30, s49, s28
	s_cselect_b32 s29, s17, s52
	s_cselect_b32 s28, s50, s51
	v_lshl_add_u64 v[232:233], s[26:27], 0, v[138:139]
	s_add_i32 m0, s25, 0xc000
	ds_read_b128 v[200:203], v164
	ds_read_b128 v[204:207], v164 offset:1024
	ds_read_b128 v[208:211], v164 offset:2048
	ds_read_b128 v[212:215], v164 offset:3072
	ds_read_b128 v[216:219], v164 offset:4096
	ds_read_b128 v[220:223], v164 offset:5120
	ds_read_b128 v[224:227], v164 offset:6144
	ds_read_b128 v[228:231], v164 offset:7168
	global_load_lds_dwordx4 v[232:233], off
	v_lshl_add_u64 v[232:233], s[26:27], 0, v[140:141]
	s_add_i32 m0, s25, 0xe000
	s_nop 0
	global_load_lds_dwordx4 v[232:233], off
	s_waitcnt vmcnt(8)
	s_waitcnt lgkmcnt(0)
	s_barrier
	s_waitcnt lgkmcnt(0)
	v_mfma_f32_16x16x32_bf16 v[126:129], v[146:149], v[200:203], v[126:129]
	v_mfma_f32_16x16x32_bf16 v[122:125], v[174:177], v[200:203], v[122:125]
	v_mfma_f32_16x16x32_bf16 v[118:121], v[146:149], v[208:211], v[118:121]
	v_mfma_f32_16x16x32_bf16 v[110:113], v[174:177], v[208:211], v[110:113]
	v_mfma_f32_16x16x32_bf16 v[102:105], v[146:149], v[216:219], v[102:105]
	v_mfma_f32_16x16x32_bf16 v[94:97], v[174:177], v[216:219], v[94:97]
	v_mfma_f32_16x16x32_bf16 v[86:89], v[146:149], v[224:227], v[86:89]
	v_mfma_f32_16x16x32_bf16 v[78:81], v[174:177], v[224:227], v[78:81]
	v_mfma_f32_16x16x32_bf16 v[126:129], v[170:173], v[204:207], v[126:129]
	v_mfma_f32_16x16x32_bf16 v[122:125], v[178:181], v[204:207], v[122:125]
	v_mfma_f32_16x16x32_bf16 v[118:121], v[170:173], v[212:215], v[118:121]
	v_mfma_f32_16x16x32_bf16 v[110:113], v[178:181], v[212:215], v[110:113]
	v_mfma_f32_16x16x32_bf16 v[102:105], v[170:173], v[220:223], v[102:105]
	v_mfma_f32_16x16x32_bf16 v[94:97], v[178:181], v[220:223], v[94:97]
	v_mfma_f32_16x16x32_bf16 v[86:89], v[170:173], v[228:231], v[86:89]
	v_mfma_f32_16x16x32_bf16 v[78:81], v[178:181], v[228:231], v[78:81]
	v_mfma_f32_16x16x32_bf16 v[114:117], v[182:185], v[200:203], v[114:117]
	v_mfma_f32_16x16x32_bf16 v[106:109], v[192:195], v[200:203], v[106:109]
	v_mfma_f32_16x16x32_bf16 v[98:101], v[182:185], v[208:211], v[98:101]
	v_mfma_f32_16x16x32_bf16 v[90:93], v[192:195], v[208:211], v[90:93]
	v_mfma_f32_16x16x32_bf16 v[82:85], v[182:185], v[216:219], v[82:85]
	v_mfma_f32_16x16x32_bf16 v[74:77], v[192:195], v[216:219], v[74:77]
	v_mfma_f32_16x16x32_bf16 v[70:73], v[182:185], v[224:227], v[70:73]
	v_mfma_f32_16x16x32_bf16 v[66:69], v[192:195], v[224:227], v[66:69]
	v_mfma_f32_16x16x32_bf16 v[114:117], v[188:191], v[204:207], v[114:117]
	v_mfma_f32_16x16x32_bf16 v[106:109], v[196:199], v[204:207], v[106:109]
	v_mfma_f32_16x16x32_bf16 v[98:101], v[188:191], v[212:215], v[98:101]
	v_mfma_f32_16x16x32_bf16 v[90:93], v[196:199], v[212:215], v[90:93]
	v_mfma_f32_16x16x32_bf16 v[82:85], v[188:191], v[220:223], v[82:85]
	v_mfma_f32_16x16x32_bf16 v[74:77], v[196:199], v[220:223], v[74:77]
	v_mfma_f32_16x16x32_bf16 v[70:73], v[188:191], v[228:231], v[70:73]
	v_mfma_f32_16x16x32_bf16 v[66:69], v[196:199], v[228:231], v[66:69]
	s_barrier
	s_add_i32 s54, s46, s36
	v_lshl_add_u64 v[232:233], s[28:29], 0, v[134:135]
	s_mov_b32 m0, s54
	ds_read_b128 v[200:203], v164 offset:16384
	ds_read_b128 v[204:207], v164 offset:17408
	ds_read_b128 v[208:211], v164 offset:18432
	ds_read_b128 v[212:215], v164 offset:19456
	ds_read_b128 v[216:219], v164 offset:20480
	ds_read_b128 v[220:223], v164 offset:21504
	ds_read_b128 v[224:227], v164 offset:22528
	ds_read_b128 v[228:231], v164 offset:23552
	global_load_lds_dwordx4 v[232:233], off
	s_add_i32 m0, s54, 0x2000
	s_add_u32 s54, s28, 0x80000
	v_lshl_add_u64 v[234:235], s[28:29], 0, v[130:131]
	s_addc_u32 s55, s29, 0
	s_add_i32 s57, s47, s36
	global_load_lds_dwordx4 v[234:235], off
	v_lshl_add_u64 v[236:237], s[54:55], 0, v[134:135]
	s_mov_b32 m0, s57
	v_lshl_add_u64 v[238:239], s[30:31], 0, v[132:133]
	global_load_lds_dwordx4 v[236:237], off
	v_lshl_add_u64 v[236:237], s[54:55], 0, v[130:131]
	s_add_i32 m0, s57, 0x2000
	s_nop 0
	global_load_lds_dwordx4 v[236:237], off
	v_lshl_add_u64 v[236:237], s[30:31], 0, v[136:137]
	s_mov_b32 m0, s25
	s_nop 0
	global_load_lds_dwordx4 v[236:237], off
	s_mov_b32 m0, s39
	s_nop 0
	global_load_lds_dwordx4 v[238:239], off
	s_waitcnt vmcnt(8)
	s_waitcnt lgkmcnt(0)
	s_barrier
	s_waitcnt lgkmcnt(0)
	v_mfma_f32_16x16x32_bf16 v[62:65], v[146:149], v[200:203], v[62:65]
	v_mfma_f32_16x16x32_bf16 v[58:61], v[174:177], v[200:203], v[58:61]
	v_mfma_f32_16x16x32_bf16 v[54:57], v[146:149], v[208:211], v[54:57]
	v_mfma_f32_16x16x32_bf16 v[46:49], v[174:177], v[208:211], v[46:49]
	v_mfma_f32_16x16x32_bf16 v[38:41], v[146:149], v[216:219], v[38:41]
	v_mfma_f32_16x16x32_bf16 v[30:33], v[174:177], v[216:219], v[30:33]
	v_mfma_f32_16x16x32_bf16 v[22:25], v[146:149], v[224:227], v[22:25]
	v_mfma_f32_16x16x32_bf16 v[14:17], v[174:177], v[224:227], v[14:17]
	v_mfma_f32_16x16x32_bf16 v[62:65], v[170:173], v[204:207], v[62:65]
	v_mfma_f32_16x16x32_bf16 v[58:61], v[178:181], v[204:207], v[58:61]
	v_mfma_f32_16x16x32_bf16 v[54:57], v[170:173], v[212:215], v[54:57]
	v_mfma_f32_16x16x32_bf16 v[46:49], v[178:181], v[212:215], v[46:49]
	v_mfma_f32_16x16x32_bf16 v[38:41], v[170:173], v[220:223], v[38:41]
	v_mfma_f32_16x16x32_bf16 v[30:33], v[178:181], v[220:223], v[30:33]
	v_mfma_f32_16x16x32_bf16 v[22:25], v[170:173], v[228:231], v[22:25]
	v_mfma_f32_16x16x32_bf16 v[14:17], v[178:181], v[228:231], v[14:17]
	v_mfma_f32_16x16x32_bf16 v[50:53], v[182:185], v[200:203], v[50:53]
	v_mfma_f32_16x16x32_bf16 v[42:45], v[192:195], v[200:203], v[42:45]
	v_mfma_f32_16x16x32_bf16 v[34:37], v[182:185], v[208:211], v[34:37]
	v_mfma_f32_16x16x32_bf16 v[26:29], v[192:195], v[208:211], v[26:29]
	v_mfma_f32_16x16x32_bf16 v[18:21], v[182:185], v[216:219], v[18:21]
	v_mfma_f32_16x16x32_bf16 v[10:13], v[192:195], v[216:219], v[10:13]
	v_mfma_f32_16x16x32_bf16 v[6:9], v[182:185], v[224:227], v[6:9]
	v_mfma_f32_16x16x32_bf16 v[2:5], v[192:195], v[224:227], v[2:5]
	v_mfma_f32_16x16x32_bf16 v[50:53], v[188:191], v[204:207], v[50:53]
	v_mfma_f32_16x16x32_bf16 v[42:45], v[196:199], v[204:207], v[42:45]
	v_mfma_f32_16x16x32_bf16 v[34:37], v[188:191], v[212:215], v[34:37]
	v_mfma_f32_16x16x32_bf16 v[26:29], v[196:199], v[212:215], v[26:29]
	v_mfma_f32_16x16x32_bf16 v[18:21], v[188:191], v[220:223], v[18:21]
	v_mfma_f32_16x16x32_bf16 v[10:13], v[196:199], v[220:223], v[10:13]
	v_mfma_f32_16x16x32_bf16 v[6:9], v[188:191], v[228:231], v[6:9]
	v_mfma_f32_16x16x32_bf16 v[2:5], v[196:199], v[228:231], v[2:5]
	s_barrier
	s_add_i32 s54, 0, 0x18000
	v_add_u32_e32 v146, s54, v152
	v_add_u32_e32 v169, s54, v153
	s_add_i32 s55, 0, 0x1c000
	ds_read_b128 v[146:149], v146
	ds_read_b128 v[170:173], v169
	ds_read_b128 v[174:177], v165
	ds_read_b128 v[178:181], v166
	v_add_u32_e32 v169, s55, v152
	v_add_u32_e32 v187, s55, v153
	ds_read_b128 v[182:185], v169
	ds_read_b128 v[188:191], v187
	ds_read_b128 v[192:195], v167
	ds_read_b128 v[196:199], v168
	s_add_u32 s30, s30, 0x80000
	s_addc_u32 s31, s31, 0
	s_mov_b32 m0, s40
	v_lshl_add_u64 v[240:241], s[30:31], 0, v[136:137]
	ds_read_b128 v[200:203], v164 offset:32768
	ds_read_b128 v[204:207], v164 offset:33792
	ds_read_b128 v[208:211], v164 offset:34816
	ds_read_b128 v[212:215], v164 offset:35840
	ds_read_b128 v[216:219], v164 offset:36864
	ds_read_b128 v[220:223], v164 offset:37888
	ds_read_b128 v[224:227], v164 offset:38912
	ds_read_b128 v[228:231], v164 offset:39936
	global_load_lds_dwordx4 v[240:241], off
	v_lshl_add_u64 v[240:241], s[30:31], 0, v[132:133]
	s_mov_b32 m0, s41
	s_nop 0
	global_load_lds_dwordx4 v[240:241], off
	s_waitcnt vmcnt(8)
	s_waitcnt lgkmcnt(0)
	s_barrier
	s_waitcnt lgkmcnt(0)
	v_mfma_f32_16x16x32_bf16 v[126:129], v[146:149], v[200:203], v[126:129]
	v_mfma_f32_16x16x32_bf16 v[122:125], v[174:177], v[200:203], v[122:125]
	v_mfma_f32_16x16x32_bf16 v[118:121], v[146:149], v[208:211], v[118:121]
	v_mfma_f32_16x16x32_bf16 v[110:113], v[174:177], v[208:211], v[110:113]
	v_mfma_f32_16x16x32_bf16 v[102:105], v[146:149], v[216:219], v[102:105]
	v_mfma_f32_16x16x32_bf16 v[94:97], v[174:177], v[216:219], v[94:97]
	v_mfma_f32_16x16x32_bf16 v[86:89], v[146:149], v[224:227], v[86:89]
	v_mfma_f32_16x16x32_bf16 v[78:81], v[174:177], v[224:227], v[78:81]
	v_mfma_f32_16x16x32_bf16 v[126:129], v[170:173], v[204:207], v[126:129]
	v_mfma_f32_16x16x32_bf16 v[122:125], v[178:181], v[204:207], v[122:125]
	v_mfma_f32_16x16x32_bf16 v[118:121], v[170:173], v[212:215], v[118:121]
	v_mfma_f32_16x16x32_bf16 v[110:113], v[178:181], v[212:215], v[110:113]
	v_mfma_f32_16x16x32_bf16 v[102:105], v[170:173], v[220:223], v[102:105]
	v_mfma_f32_16x16x32_bf16 v[94:97], v[178:181], v[220:223], v[94:97]
	v_mfma_f32_16x16x32_bf16 v[86:89], v[170:173], v[228:231], v[86:89]
	v_mfma_f32_16x16x32_bf16 v[78:81], v[178:181], v[228:231], v[78:81]
	v_mfma_f32_16x16x32_bf16 v[114:117], v[182:185], v[200:203], v[114:117]
	v_mfma_f32_16x16x32_bf16 v[106:109], v[192:195], v[200:203], v[106:109]
	v_mfma_f32_16x16x32_bf16 v[98:101], v[182:185], v[208:211], v[98:101]
	v_mfma_f32_16x16x32_bf16 v[90:93], v[192:195], v[208:211], v[90:93]
	v_mfma_f32_16x16x32_bf16 v[82:85], v[182:185], v[216:219], v[82:85]
	v_mfma_f32_16x16x32_bf16 v[74:77], v[192:195], v[216:219], v[74:77]
	v_mfma_f32_16x16x32_bf16 v[70:73], v[182:185], v[224:227], v[70:73]
	v_mfma_f32_16x16x32_bf16 v[66:69], v[192:195], v[224:227], v[66:69]
	v_mfma_f32_16x16x32_bf16 v[114:117], v[188:191], v[204:207], v[114:117]
	v_mfma_f32_16x16x32_bf16 v[106:109], v[196:199], v[204:207], v[106:109]
	v_mfma_f32_16x16x32_bf16 v[98:101], v[188:191], v[212:215], v[98:101]
	v_mfma_f32_16x16x32_bf16 v[90:93], v[196:199], v[212:215], v[90:93]
	v_mfma_f32_16x16x32_bf16 v[82:85], v[188:191], v[220:223], v[82:85]
	v_mfma_f32_16x16x32_bf16 v[74:77], v[196:199], v[220:223], v[74:77]
	v_mfma_f32_16x16x32_bf16 v[70:73], v[188:191], v[228:231], v[70:73]
	v_mfma_f32_16x16x32_bf16 v[66:69], v[196:199], v[228:231], v[66:69]
	s_barrier
	s_add_i32 s30, s54, s36
	v_lshl_add_u64 v[232:233], v[232:233], 0, s[12:13]
	s_mov_b32 m0, s30
	ds_read_b128 v[200:203], v164 offset:49152
	ds_read_b128 v[204:207], v164 offset:50176
	ds_read_b128 v[208:211], v164 offset:51200
	ds_read_b128 v[212:215], v164 offset:52224
	ds_read_b128 v[216:219], v164 offset:53248
	ds_read_b128 v[220:223], v164 offset:54272
	ds_read_b128 v[224:227], v164 offset:55296
	ds_read_b128 v[228:231], v164 offset:56320
	global_load_lds_dwordx4 v[232:233], off
	s_add_i32 m0, s30, 0x2000
	s_add_u32 s28, s28, 0x80080
	v_lshl_add_u64 v[232:233], v[234:235], 0, s[12:13]
	s_addc_u32 s29, s29, 0
	s_add_i32 s30, s55, s36
	global_load_lds_dwordx4 v[232:233], off
	v_lshl_add_u64 v[232:233], s[28:29], 0, v[134:135]
	s_mov_b32 m0, s30
	s_nop 0
	global_load_lds_dwordx4 v[232:233], off
	v_lshl_add_u64 v[232:233], s[28:29], 0, v[130:131]
	s_add_i32 m0, s30, 0x2000
	s_nop 0
	global_load_lds_dwordx4 v[232:233], off
	v_lshl_add_u64 v[232:233], v[236:237], 0, s[12:13]
	s_mov_b32 m0, s43
	s_nop 0
	global_load_lds_dwordx4 v[232:233], off
	v_lshl_add_u64 v[232:233], v[238:239], 0, s[12:13]
	s_mov_b32 m0, s44
	s_nop 0
	global_load_lds_dwordx4 v[232:233], off
	s_waitcnt vmcnt(8)
	s_waitcnt lgkmcnt(0)
	s_barrier
	s_waitcnt lgkmcnt(0)
	v_mfma_f32_16x16x32_bf16 v[62:65], v[146:149], v[200:203], v[62:65]
	v_mfma_f32_16x16x32_bf16 v[58:61], v[174:177], v[200:203], v[58:61]
	v_mfma_f32_16x16x32_bf16 v[54:57], v[146:149], v[208:211], v[54:57]
	v_mfma_f32_16x16x32_bf16 v[46:49], v[174:177], v[208:211], v[46:49]
	v_mfma_f32_16x16x32_bf16 v[38:41], v[146:149], v[216:219], v[38:41]
	v_mfma_f32_16x16x32_bf16 v[30:33], v[174:177], v[216:219], v[30:33]
	v_mfma_f32_16x16x32_bf16 v[22:25], v[146:149], v[224:227], v[22:25]
	v_mfma_f32_16x16x32_bf16 v[14:17], v[174:177], v[224:227], v[14:17]
	v_mfma_f32_16x16x32_bf16 v[62:65], v[170:173], v[204:207], v[62:65]
	v_mfma_f32_16x16x32_bf16 v[58:61], v[178:181], v[204:207], v[58:61]
	v_mfma_f32_16x16x32_bf16 v[54:57], v[170:173], v[212:215], v[54:57]
	v_mfma_f32_16x16x32_bf16 v[46:49], v[178:181], v[212:215], v[46:49]
	v_mfma_f32_16x16x32_bf16 v[38:41], v[170:173], v[220:223], v[38:41]
	v_mfma_f32_16x16x32_bf16 v[30:33], v[178:181], v[220:223], v[30:33]
	v_mfma_f32_16x16x32_bf16 v[22:25], v[170:173], v[228:231], v[22:25]
	v_mfma_f32_16x16x32_bf16 v[14:17], v[178:181], v[228:231], v[14:17]
	v_mfma_f32_16x16x32_bf16 v[50:53], v[182:185], v[200:203], v[50:53]
	v_mfma_f32_16x16x32_bf16 v[42:45], v[192:195], v[200:203], v[42:45]
	v_mfma_f32_16x16x32_bf16 v[34:37], v[182:185], v[208:211], v[34:37]
	v_mfma_f32_16x16x32_bf16 v[26:29], v[192:195], v[208:211], v[26:29]
	v_mfma_f32_16x16x32_bf16 v[18:21], v[182:185], v[216:219], v[18:21]
	v_mfma_f32_16x16x32_bf16 v[10:13], v[192:195], v[216:219], v[10:13]
	v_mfma_f32_16x16x32_bf16 v[6:9], v[182:185], v[224:227], v[6:9]
	v_mfma_f32_16x16x32_bf16 v[2:5], v[192:195], v[224:227], v[2:5]
	v_mfma_f32_16x16x32_bf16 v[50:53], v[188:191], v[204:207], v[50:53]
	v_mfma_f32_16x16x32_bf16 v[42:45], v[196:199], v[204:207], v[42:45]
	v_mfma_f32_16x16x32_bf16 v[34:37], v[188:191], v[212:215], v[34:37]
	v_mfma_f32_16x16x32_bf16 v[26:29], v[196:199], v[212:215], v[26:29]
	v_mfma_f32_16x16x32_bf16 v[18:21], v[188:191], v[220:223], v[18:21]
	v_mfma_f32_16x16x32_bf16 v[10:13], v[196:199], v[220:223], v[10:13]
	v_mfma_f32_16x16x32_bf16 v[6:9], v[188:191], v[228:231], v[6:9]
	v_mfma_f32_16x16x32_bf16 v[2:5], v[196:199], v[228:231], v[2:5]
	s_barrier
	s_add_i32 s53, s53, 2
	s_add_u32 s26, s26, 0x100
	s_addc_u32 s27, s27, 0
	s_add_u32 s51, s51, 0x100
	s_addc_u32 s52, s52, 0
	s_cmp_gt_u32 s53, 29
	s_cbranch_scc0 .LBB0_86
	s_and_b64 vcc, exec, s[14:15]
	s_cbranch_vccz .LBB0_89
	s_barrier

.LBB0_93:
	s_setprio 0
	s_lshl_b32 s8, s33, 3
	s_abs_i32 s4, s8
	v_cvt_f32_u32_e32 v2, s4
	s_sub_i32 s10, 0, s4
	s_add_i32 s5, s8, 0x7ff
	s_xor_b32 s9, s5, s8
	v_rcp_iflag_f32_e32 v2, v2
	s_abs_i32 s5, s5
	s_ashr_i32 s9, s9, 31
	v_mul_f32_e32 v2, 0x4f7ffffe, v2
	v_cvt_u32_f32_e32 v2, v2
	s_nop 0
	v_readfirstlane_b32 s11, v2
	s_mul_i32 s10, s10, s11
	s_mul_hi_u32 s10, s11, s10
	s_add_i32 s11, s11, s10
	s_mul_hi_u32 s10, s5, s11
	s_mul_i32 s11, s10, s4
	s_sub_i32 s5, s5, s11
	s_add_i32 s12, s10, 1
	s_sub_i32 s11, s5, s4
	s_cmp_ge_u32 s5, s4
	s_cselect_b32 s10, s12, s10
	s_cselect_b32 s5, s11, s5
	s_add_i32 s11, s10, 1
	s_cmp_ge_u32 s5, s4
	s_cselect_b32 s4, s11, s10
	s_xor_b32 s4, s4, s9
	s_sub_i32 s9, s4, s9
	s_cmp_lt_i32 s9, 1
	s_cbranch_scc1 .LBB0_98
	v_readlane_b32 s4, v254, 0
	s_mov_b32 s2, s4
	s_lshl_b32 s4, s4, 3
	s_add_i32 s10, s82, s4
	v_and_b32_e32 v6, 31, v0
	s_mul_i32 s4, s82, 0x1080
	v_lshlrev_b32_e32 v2, 12, v1
	v_mov_b32_e32 v3, 0
	s_add_i32 s4, s4, 0
	v_lshl_add_u64 v[4:5], s[96:97], 0, v[2:3]
	v_lshlrev_b32_e32 v2, 4, v6
	v_and_b32_e32 v7, 7, v0
	v_lshl_add_u64 v[18:19], s[6:7], 0, v[2:3]
	v_add_u32_e32 v10, s4, v2
	s_movk_i32 s6, 0x210
	v_mov_b32_e32 v2, s4
	v_readlane_b32 s5, v254, 1
	v_mad_u32_u24 v11, v7, s6, v2
	v_lshlrev_b32_e32 v2, 2, v150
	v_lshlrev_b32_e32 v6, 4, v7
	v_lshl_add_u64 v[8:9], s[96:97], 0, v[2:3]
	s_mov_b64 s[4:5], 0x4e000000
	v_mov_b32_e32 v7, v3
	v_lshl_add_u64 v[20:21], v[8:9], 0, s[4:5]
	v_lshl_add_u64 v[2:3], v[4:5], 0, v[6:7]
	s_mov_b64 s[4:5], 0x2e00000
	v_and_b32_e32 v12, 48, v0
	v_lshl_add_u64 v[22:23], v[2:3], 0, s[4:5]
	s_add_i32 s4, 0, 0x12400
	v_lshrrev_b32_e32 v24, 5, v186
	v_mul_u32_u24_e32 v3, 0x210, v150
	v_mov_b32_e32 v4, s4
	v_add_u32_e32 v7, 0, v12
	v_mul_u32_u24_e32 v2, 0x210, v24
	v_mad_u32_u24 v4, v1, s6, v4
	v_add3_u32 v26, s4, v12, v3
	v_mad_u32_u24 v5, v1, s6, 0
	v_add_u32_e32 v8, 0xa000, v7
	v_mad_u32_u24 v1, v150, s6, v7
	v_add_u32_e32 v9, 0xa040, v7
	v_add_u32_e32 v13, 0xa080, v7
	v_add_u32_e32 v14, 0xa0c0, v7
	v_add_u32_e32 v15, 0xa100, v7
	v_add_u32_e32 v16, 0xa140, v7
	v_add_u32_e32 v17, 0xa180, v7
	v_add_u32_e32 v7, 0xa1c0, v7
	s_lshl_b32 s4, s2, 6
	s_lshl_b32 s5, s82, 3
	v_cmp_gt_u32_e32 vcc, 32, v186
	v_and_b32_e32 v25, 12, v151
	s_add_i32 s6, s4, s5
	s_lshl_b32 s7, s33, 6
	v_add_u32_e32 v27, v5, v6
	v_add_u32_e32 v28, v10, v2
	v_add_u32_e32 v29, v11, v12
	v_add_u32_e32 v30, v8, v3
	v_add_u32_e32 v31, v9, v3
	v_add_u32_e32 v32, v13, v3
	v_add_u32_e32 v33, v14, v3
	v_add_u32_e32 v34, v15, v3
	v_add_u32_e32 v35, v16, v3
	v_add_u32_e32 v36, v17, v3
	v_add_u32_e32 v37, v7, v3
	v_add_u32_e32 v38, v4, v6
	s_branch .LBB0_96
